# MoBA unit set-up: Q fragments and K/V tiles 0-2 requested before the gating pass
# baseline (speedup 1.0000x reference)
; #define LAS __attribute__((address_space(3)))
; #define ATT_DMA(t, slot) do { glds16(ksrc + (long)(t) * tstep, (unsigned)__builtin_amdgcn_readfirstlane(kdst + (slot))); glds16(vsrc + (long)(t) * tstep, (unsigned)__builtin_amdgcn_readfirstlane(vdst + (slot))); } while (0)
; __device__ __forceinline__ void unpack8(const v4u w, float* f) { f[0] = bflo(w.x); f[1] = bfhi(w.x); f[2] = bflo(w.y); f[3] = bfhi(w.y); f[4] = bflo(w.z); f[5] = bfhi(w.z); f[6] = bflo(w.w); f[7] = bfhi(w.w); }
; template <class BIAS>
; __device__ __forceinline__ void attn_tiles(char* shm, const UnitIO& io, int t_begin, int t_end, const BIAS& B, int tid) {
;     ...
;     { const bf16* qp = io.Q + (long)r32 * io.qstride + hi * 8;
; #pragma unroll
;       for (int d0 = 0; d0 < 4; ++d0) qr[d0] = *reinterpret_cast<const bf16x8*>(qp + d0 * 16); }
;     ATT_DMA(t_begin, 0);
;     asm volatile("" :: "v"(qr[0]), "v"(qr[1]), "v"(qr[2]), "v"(qr[3]));
;     const int nt_ = t_end - t_begin; if (nt_ > 1) ATT_DMA(t_begin + 1, SLOTB); if (nt_ > 2) ATT_DMA(t_begin + 2, 2 * SLOTB);
; __device__ __forceinline__ void moba_unit(Frame& F, const AttnBufs& A, int b, int h, int qb) {
;     ...
;     for (int i = tid; i < 1024; i += 512) { const int j = i >> 6, d = i & 63; float v = 0.f;
;         if (j < qb) { const float* p = A.KMP + ((size_t)((b * 16 + j) * 4 + h) * 2) * 64 + d; v = p[0] + p[64]; } KM[i] = v; }
;     const size_t row0 = (size_t)b * SEQ + qb * 256 + w * 32;
;     const size_t bo = (size_t)b * BADJ;
;     const bf16* Qw = A.Q + bo + row0 * DM + h * 64;
;     float qf[32];
;     { const bf16* qp = Qw + (size_t)r32 * DM + hi * 8;
; #pragma unroll
;       for (int d0 = 0; d0 < 4; ++d0) { const v4u wv = *(const v4u*)(qp + d0 * 16); unpack8(wv, qf + 8 * d0); } }
;     __syncthreads();
;     float g0 = -INFINITY, g1 = -INFINITY, g2 = -INFINITY; int i0 = -1, i1 = -1, i2 = -1;
; #pragma unroll 1
;     for (int j = 0; j < qb; ++j) {
;         float dot = 0.f;
; #pragma unroll
;         for (int d0 = 0; d0 < 4; ++d0) { const f32x4 ka = *(const LAS f32x4*)(KM + j * 64 + d0 * 16 + hi * 8), kb = *(const LAS f32x4*)(KM + j * 64 + d0 * 16 + hi * 8 + 4);
; #pragma unroll
;             for (int e = 0; e < 4; ++e) { dot += qf[8 * d0 + e] * ka[e]; dot += qf[8 * d0 + 4 + e] * kb[e]; } }
.LBB0_283:
	s_or_b64 exec, exec, s[8:9]
	s_xor_b64 s[8:9], s[4:5], -1
	s_lshl_b32 s22, s20, 8
	v_readlane_b32 s4, v254, 36
	s_add_u32 s10, s4, s22
	v_readlane_b32 s4, v254, 40
	s_addc_u32 s11, s4, 0
	s_lshl_b64 s[4:5], s[10:11], 11
	v_readlane_b32 s12, v254, 43
	s_add_u32 s4, s12, s4
	v_readlane_b32 s12, v254, 46
	s_addc_u32 s5, s12, s5
	v_mov_b32_e32 v169, v1
	v_lshl_add_u64 v[2:3], s[4:5], 0, v[168:169]
	v_mov_b32_e32 v171, v1
	v_lshl_add_u64 v[2:3], v[2:3], 0, v[170:171]
	flat_load_dwordx4 v[14:17], v[2:3]
	flat_load_dwordx4 v[10:13], v[2:3] offset:32
	flat_load_dwordx4 v[6:9], v[2:3] offset:64
	s_nop 0
	flat_load_dwordx4 v[2:5], v[2:3] offset:96
	v_lshlrev_b32_e32 v148, 1, v154
	v_mov_b32_e32 v149, v1
	v_lshl_add_u64 v[212:213], s[4:5], 0, v[132:133]
	v_lshl_add_u64 v[212:213], v[212:213], 0, v[148:149]
	flat_load_dwordx4 v[66:69], v[212:213]
	flat_load_dwordx4 v[70:73], v[212:213] offset:32
	flat_load_dwordx4 v[74:77], v[212:213] offset:64
	flat_load_dwordx4 v[78:81], v[212:213] offset:96
	v_readfirstlane_b32 s27, v232
	s_ashr_i32 s16, s27, 6
	s_lshl_b32 s12, s16, 4
	v_and_or_b32 v222, s12, 48, v178
	s_ashr_i32 s12, s27, 3
	s_lshl_b32 s14, s16, 3
	s_andn2_b32 s12, s12, 31
	s_ashr_i32 s15, s14, 31
	s_ashr_i32 s13, s12, 31
	v_lshlrev_b32_e32 v222, 11, v222
	v_mov_b32_e32 v223, v1
	s_lshl_b64 s[100:101], s[14:15], 1
	v_lshl_add_u64 v[222:223], s[30:31], 0, v[222:223]
	s_lshl_b64 s[12:13], s[12:13], 1
	s_lshl_b32 s29, s16, 10
	v_lshl_add_u64 v[212:213], v[156:157], 0, s[100:101]
	v_lshl_add_u64 v[212:213], v[212:213], 0, v[244:245]
	v_lshl_add_u64 v[222:223], v[222:223], 0, s[12:13]
	v_lshlrev_b32_e32 v150, 1, v144
	v_mov_b32_e32 v151, v1
	v_lshl_add_u64 v[222:223], v[222:223], 0, v[150:151]
	s_add_i32 s33, s29, 0x8000
	s_mov_b64 s[100:101], 0x20000
	s_mov_b32 m0, s29
	s_add_i32 s12, s29, 0x2000
	global_load_lds_dwordx4 v[212:213], off
	s_mov_b32 m0, s33
	s_add_i32 s13, s33, 0x2000
	global_load_lds_dwordx4 v[222:223], off
	v_lshl_add_u64 v[212:213], v[212:213], 0, s[100:101]
	v_lshl_add_u64 v[222:223], v[222:223], 0, s[100:101]
	s_mov_b32 m0, s12
	s_add_i32 s12, s29, 0x4000
	global_load_lds_dwordx4 v[212:213], off
	s_mov_b32 m0, s13
	s_add_i32 s13, s33, 0x4000
	global_load_lds_dwordx4 v[222:223], off
	v_lshl_add_u64 v[212:213], v[212:213], 0, s[100:101]
	v_lshl_add_u64 v[222:223], v[222:223], 0, s[100:101]
	s_mov_b32 m0, s12
	s_nop 0
	global_load_lds_dwordx4 v[212:213], off
	s_mov_b32 m0, s13
	s_nop 0
	global_load_lds_dwordx4 v[222:223], off
	s_cmp_eq_u32 s20, 0
	s_waitcnt vmcnt(0) lgkmcnt(0)
	s_barrier
	s_cbranch_scc1 .LBB0_293
	v_lshlrev_b32_e32 v18, 16, v14
	v_and_b32_e32 v14, 0xffff0000, v14
	v_lshlrev_b32_e32 v19, 16, v15
	v_and_b32_e32 v15, 0xffff0000, v15
	v_lshlrev_b32_e32 v20, 16, v16
	v_and_b32_e32 v16, 0xffff0000, v16
	v_lshlrev_b32_e32 v21, 16, v17
	v_and_b32_e32 v17, 0xffff0000, v17
	v_lshlrev_b32_e32 v22, 16, v10
	v_and_b32_e32 v23, 0xffff0000, v10
	v_lshlrev_b32_e32 v24, 16, v11
	v_and_b32_e32 v25, 0xffff0000, v11
	v_lshlrev_b32_e32 v26, 16, v12
	v_and_b32_e32 v12, 0xffff0000, v12
	v_lshlrev_b32_e32 v27, 16, v13
	v_and_b32_e32 v13, 0xffff0000, v13
	v_lshlrev_b32_e32 v28, 16, v6
	v_and_b32_e32 v29, 0xffff0000, v6
	v_lshlrev_b32_e32 v30, 16, v7
	v_and_b32_e32 v31, 0xffff0000, v7
	v_lshlrev_b32_e32 v32, 16, v8
	v_and_b32_e32 v33, 0xffff0000, v8
	v_lshlrev_b32_e32 v34, 16, v9
	v_and_b32_e32 v35, 0xffff0000, v9
	v_lshlrev_b32_e32 v7, 16, v2
	v_lshlrev_b32_e32 v6, 16, v4
	v_and_b32_e32 v9, 0xffff0000, v2
	v_and_b32_e32 v8, 0xffff0000, v4
	v_lshlrev_b32_e32 v11, 16, v3
	v_lshlrev_b32_e32 v10, 16, v5
	v_and_b32_e32 v3, 0xffff0000, v3
	v_and_b32_e32 v2, 0xffff0000, v5
	v_mov_b32_e32 v39, 0xff800000
	v_mov_b32_e32 v38, -1
	s_mov_b32 s23, 0
	s_mov_b32 s26, 0
	v_mov_b32_e32 v4, -1
	v_mov_b32_e32 v5, -1
	v_mov_b32_e32 v36, 0xff800000
	v_mov_b32_e32 v37, 0xff800000
.LBB0_285:
	v_add_u32_e32 v48, s23, v174
	v_add_u32_e32 v49, 0x18800, v48
	ds_read_b128 v[98:101], v49
	ds_read_b128 v[102:105], v49 offset:16
	ds_read_b128 v[82:85], v49 offset:64
	ds_read_b128 v[86:89], v49 offset:80
	ds_read_b128 v[90:93], v49 offset:128
	ds_read_b128 v[94:97], v49 offset:144
	ds_read_b128 v[40:43], v49 offset:192
	ds_read_b128 v[44:47], v49 offset:208
	s_waitcnt lgkmcnt(7)
	v_fma_f32 v50, v98, v18, 0
	s_waitcnt lgkmcnt(6)
	v_fmac_f32_e32 v50, v102, v20
	v_fmac_f32_e32 v50, v99, v14
	v_fmac_f32_e32 v50, v103, v16
	v_fmac_f32_e32 v50, v100, v19
	v_fmac_f32_e32 v50, v104, v21
	v_fmac_f32_e32 v50, v101, v15
	v_fmac_f32_e32 v50, v105, v17
	s_waitcnt lgkmcnt(5)
	v_fmac_f32_e32 v50, v82, v22
	s_waitcnt lgkmcnt(4)
	v_fmac_f32_e32 v50, v86, v26
	v_fmac_f32_e32 v50, v83, v23
	v_fmac_f32_e32 v50, v87, v12
	v_fmac_f32_e32 v50, v84, v24
	v_fmac_f32_e32 v50, v88, v27
	v_fmac_f32_e32 v50, v85, v25
	v_fmac_f32_e32 v50, v89, v13
	s_waitcnt lgkmcnt(3)
	v_fmac_f32_e32 v50, v90, v28
	s_waitcnt lgkmcnt(2)
	v_fmac_f32_e32 v50, v94, v32
	v_fmac_f32_e32 v50, v91, v29
	v_fmac_f32_e32 v50, v95, v33
	v_fmac_f32_e32 v50, v92, v30
	v_fmac_f32_e32 v50, v96, v34
	v_fmac_f32_e32 v50, v93, v31
	v_fmac_f32_e32 v50, v97, v35
	s_waitcnt lgkmcnt(1)
	v_mov_b32_e32 v49, v40
	s_waitcnt lgkmcnt(0)
	v_mov_b32_e32 v48, v44
	v_pk_mul_f32 v[48:49], v[48:49], v[6:7]
	s_nop 0
	v_add_f32_e32 v40, v49, v50
	v_add_f32_e32 v44, v48, v40
	v_mov_b32_e32 v40, v45
	v_pk_mul_f32 v[40:41], v[40:41], v[8:9]
	s_nop 0
	v_add_f32_e32 v41, v41, v44
	v_add_f32_e32 v44, v40, v41
	v_mov_b32_e32 v40, v46
	v_mov_b32_e32 v41, v42
	v_pk_mul_f32 v[40:41], v[40:41], v[10:11]
	v_mov_b32_e32 v42, v47
	v_add_f32_e32 v41, v41, v44
	v_add_f32_e32 v44, v40, v41
	v_pk_mul_f32 v[40:41], v[42:43], v[2:3]
	s_nop 0
	v_add_f32_e32 v41, v41, v44
	v_add_f32_e32 v40, v40, v41
	v_mov_b32_e32 v41, v40
	s_nop 1
	v_permlane32_swap_b32_e32 v40, v41
	v_add_f32_e32 v40, v40, v41
	v_cmp_ngt_f32_e32 vcc, v40, v37
	v_mov_b32_e32 v41, s26
	s_and_saveexec_b64 s[12:13], vcc
	s_cbranch_execz .LBB0_291
	v_cmp_ngt_f32_e32 vcc, v40, v36
	v_mov_b32_e32 v42, s26
	s_and_saveexec_b64 s[14:15], vcc
	s_cbranch_execz .LBB0_290
	v_cmp_gt_f32_e32 vcc, v40, v39
	s_and_saveexec_b64 s[16:17], vcc
	v_mov_b32_e32 v38, s26
	v_mov_b32_e32 v39, v40
	s_or_b64 exec, exec, s[16:17]
	v_mov_b32_e32 v42, v4
	v_mov_b32_e32 v40, v36
	v_mov_b32_e32 v36, v39
	v_mov_b32_e32 v4, v38

; #define ATT_WAIT_BAR(N) asm volatile("s_waitcnt vmcnt(" #N ") lgkmcnt(0)\n\ts_barrier" ::: "memory")
; #define ATT_DMA(t, slot) do { glds16(ksrc + (long)(t) * tstep, (unsigned)__builtin_amdgcn_readfirstlane(kdst + (slot))); glds16(vsrc + (long)(t) * tstep, (unsigned)__builtin_amdgcn_readfirstlane(vdst + (slot))); } while (0)
; template <class BIAS>
; __device__ __forceinline__ void attn_tiles(char* shm, const UnitIO& io, int t_begin, int t_end, const BIAS& B, int tid) {
;     ...
;     bf16x8 qr[4];
;     { const bf16* qp = io.Q + (long)r32 * io.qstride + hi * 8;
; #pragma unroll
;       for (int d0 = 0; d0 < 4; ++d0) qr[d0] = *reinterpret_cast<const bf16x8*>(qp + d0 * 16); }
;     ATT_DMA(t_begin, 0);
;     asm volatile("" :: "v"(qr[0]), "v"(qr[1]), "v"(qr[2]), "v"(qr[3]));
;     const int nt_ = t_end - t_begin; if (nt_ > 1) ATT_DMA(t_begin + 1, SLOTB); if (nt_ > 2) ATT_DMA(t_begin + 2, 2 * SLOTB);
;     f32x16 o[2]; o[0] = f32x16{}; o[1] = f32x16{}; float l_reg = 0.f;
;     if (nt_ > 2) ATT_WAIT_BAR(4); else if (nt_ > 1) ATT_WAIT_BAR(2); else ATT_WAIT_BAR(0);
.LBB0_294:
	v_lshlrev_b32_e64 v2, v41, 1
	v_cmp_lt_i32_e32 vcc, -1, v41
	v_lshlrev_b32_e64 v3, v5, 1
	v_lshlrev_b32_e32 v148, 1, v154
	v_cndmask_b32_e32 v2, 0, v2, vcc
	v_cmp_lt_i32_e32 vcc, -1, v5
	v_lshlrev_b32_e64 v5, v4, 1
	v_mov_b32_e32 v149, v1
	v_cndmask_b32_e32 v3, 0, v3, vcc
	v_cmp_lt_i32_e32 vcc, -1, v4
	v_readfirstlane_b32 s27, v232
	s_ashr_i32 s16, s27, 6
	v_cndmask_b32_e32 v4, 0, v5, vcc
	v_or3_b32 v135, v3, v2, v4
	v_add_u32_e32 v2, s22, v143
	v_cvt_f32_i32_e32 v137, v2
	v_lshl_add_u64 v[2:3], s[4:5], 0, v[132:133]
	v_lshl_add_u64 v[2:3], v[2:3], 0, v[148:149]
	s_lshl_b32 s12, s16, 4
	v_and_or_b32 v4, s12, 48, v178
	s_ashr_i32 s12, s27, 3
	s_lshl_b32 s14, s16, 3
	s_andn2_b32 s12, s12, 31
	s_ashr_i32 s15, s14, 31
	s_ashr_i32 s13, s12, 31
	v_lshlrev_b32_e32 v4, 11, v4
	v_mov_b32_e32 v5, v1
	s_lshl_b64 s[4:5], s[14:15], 1
	v_lshl_add_u64 v[4:5], s[30:31], 0, v[4:5]
	s_lshl_b64 s[12:13], s[12:13], 1
	s_lshl_b32 s29, s16, 10
	v_lshl_add_u64 v[2:3], v[156:157], 0, s[4:5]
	v_lshl_add_u64 v[2:3], v[2:3], 0, v[244:245]
	v_lshl_add_u64 v[4:5], v[4:5], 0, s[12:13]
	v_lshlrev_b32_e32 v150, 1, v144
	v_mov_b32_e32 v151, v1
	s_add_i32 s33, s29, 0x8000
	v_lshl_add_u64 v[4:5], v[4:5], 0, v[150:151]
	s_mov_b64 s[22:23], 0x20000
	s_add_i32 s14, s29, 0x2000
	v_lshl_add_u64 v[6:7], v[2:3], 0, s[22:23]
	v_mov_b32_e32 v16, v1
	v_mov_b32_e32 v17, v1
	s_lshl_b32 s26, s20, 2
	v_mov_b32_e32 v8, v1
	v_mov_b32_e32 v9, v1
	v_mov_b32_e32 v10, v1
	v_mov_b32_e32 v11, v1
	v_mov_b32_e32 v12, v1
	v_mov_b32_e32 v13, v1
	v_mov_b32_e32 v14, v1
	v_mov_b32_e32 v15, v1
	s_lshl_b64 s[10:11], s[10:11], 10
	s_mov_b32 s17, 0
	s_add_i32 s28, s26, 4
	v_lshl_add_u64 v[172:173], v[166:167], 0, s[4:5]
	v_lshl_add_u64 v[172:173], v[172:173], 0, v[244:245]
	s_sub_i32 s20, 0, s26
	s_sub_i32 s24, s72, s26
	v_mov_b32_e32 v139, 0
	v_mov_b32_e32 v149, v145
	s_add_i32 s14, s33, 0x2000
	v_lshl_add_u64 v[6:7], v[4:5], 0, s[22:23]
	s_mov_b64 s[22:23], 0x40000
	s_add_i32 s14, s29, 0x4000
	v_lshl_add_u64 v[2:3], v[2:3], 0, s[22:23]
	s_add_i32 s14, s33, 0x4000
	v_lshl_add_u64 v[2:3], v[4:5], 0, s[22:23]
	s_lshl_b32 s14, s16, 15
	s_and_b32 s14, s14, 0x18000
	v_lshl_or_b32 v2, v175, 1, s14
	v_mov_b32_e32 v3, v1
	s_waitcnt vmcnt(0) lgkmcnt(0)
	s_barrier
	v_lshl_add_u64 v[2:3], s[12:13], 0, v[2:3]
	v_lshl_add_u64 v[152:153], v[164:165], 0, v[2:3]
	s_add_i32 s14, s29, 0x6000
	s_mov_b32 m0, s14
	s_add_i32 s14, s33, 0x6000
	global_load_lds_dwordx4 v[172:173], off
	s_mov_b32 m0, s14
	s_nop 0
	global_load_lds_dwordx4 v[152:153], off
	s_mov_b64 s[14:15], 0x20000
	v_lshl_add_u64 v[172:173], v[172:173], 0, s[14:15]
	v_lshl_add_u64 v[152:153], v[152:153], 0, s[14:15]
	v_mov_b32_e32 v2, v1
	v_mov_b32_e32 v3, v1
	v_mov_b32_e32 v4, v1
	v_mov_b32_e32 v5, v1
	v_mov_b32_e32 v6, v1
	v_mov_b32_e32 v7, v1
	v_mov_b64_e32 v[32:33], v[16:17]
	s_mov_b32 s22, 0
	v_mov_b64_e32 v[30:31], v[14:15]
	v_mov_b64_e32 v[28:29], v[12:13]
	v_mov_b64_e32 v[26:27], v[10:11]
	v_mov_b64_e32 v[24:25], v[8:9]
	v_mov_b64_e32 v[22:23], v[6:7]
	v_mov_b64_e32 v[20:21], v[4:5]
	v_mov_b64_e32 v[18:19], v[2:3]
	s_branch .LBB0_296
